# MLA main loop: one static s_setprio 1 for waves 4-7 (reset at loop exit)
# speedup vs baseline: 1.0351x; 1.0083x over previous
; #define WAITV(n) asm volatile("s_waitcnt vmcnt(%0)" ::"n"(n) : "memory")
; #define SBAR() do { asm volatile("s_waitcnt lgkmcnt(0)" ::: "memory"); __builtin_amdgcn_s_barrier(); asm volatile("" ::: "memory"); } while (0)
; DEV int otid() { int t = threadIdx.x; asm volatile("" : "+v"(t)); return t; }
; DEV unsigned char* ows_(unsigned char* w) { gptr_t g = (gptr_t)w; asm volatile("" : "+s"(g)); return (unsigned char*)g; }
; DEV unsigned lds_addr(LAS char* p) { return (unsigned)(uintptr_t)p; }
; #define MLA_ISSUE(t_, st_) do { const unsigned char* s_ = imgs + (size_t)(t_) * MLA_IMG + wid * (STG / 8) + lane * 16; const unsigned d_ = ldsw + (unsigned)((st_) * STG); \
;     _Pragma("unroll") for (int i_ = 0; i_ < STG / 8192; ++i_) glds16a(s_ + i_ * 1024, d_ + i_ * 1024); } while (0)
; template <int VAR> DEV void mla_unit(const Params& p, int layer, int b, int hd, int tokbase, int t0, int t1, LAS char* lds, SideJob& sj) {
;     unsigned char* ws = ows_(p.ws); const int tid = otid(), lane = tid & 63, wid = tid >> 6, r = lane & 31, h = lane >> 5;
;     constexpr int STG = MLA_IMG;
;     const float cinit = 15.0f - ((const float*)(ws + WS_SCAL))[layer * 8 + 1];
;     const int tok = tokbase + 32 * wid + r;
;     v8i qf[2];
; #pragma unroll
;     for (int sx = 0; sx < 2; ++sx) { const u32x4* q8 = (const u32x4*)(ws + WS_QC + (size_t)tok * 768 + hd * 128 + 64 * sx + 32 * h); const u32x4 a = q8[0], bq = q8[1];
;         qf[sx] = (v8i){(int)a[0], (int)a[1], (int)a[2], (int)a[3], (int)bq[0], (int)bq[1], (int)bq[2], (int)bq[3]}; }
;     const unsigned char* imgs = ws + WS_KVC + (size_t)((b * 6 + hd) * 130) * MLA_IMG;
;     const unsigned ldsw = (unsigned)__builtin_amdgcn_readfirstlane((int)(lds_addr(lds) + (unsigned)(wid * (STG / 8))));
;     ...
;     f32x16 cini, sA0, sA1, sB0, sB1, o0, o1, lacc;
; #pragma unroll
;     for (int i = 0; i < 16; ++i) { cini[i] = cinit; o0[i] = 0.f; o1[i] = 0.f; lacc[i] = 0.f; }
;     const unsigned koffl = (unsigned)(2 * h * 1024 + r * 16);
;     const unsigned voffl = (unsigned)MLA_VOFF + (unsigned)(2 * h * 1024 + r * 16);
;     const int ns = t1 - t0;
;     MLA_ISSUE(t0, 0);
;     WAITV(0); SBAR();
.LBB0_808:
	s_and_b64 vcc, exec, s[6:7]
	s_cbranch_vccz .LBB0_749
	s_ashr_i32 s2, s64, 6
	s_mul_hi_i32 s3, s2, 0x2aaaaaab
	s_lshr_b32 s6, s3, 31
	s_add_i32 s3, s3, s6
	s_mul_i32 s6, s3, 6
	s_sub_i32 s37, s2, s6
	s_lshl_b32 s6, s64, 8
	s_lshl_b32 s3, s3, 14
	s_and_b32 s6, s6, 0x3f00
	s_or_b32 s3, s3, s6
	s_mov_b64 s[6:7], s[38:39]
	v_mov_b32_e32 v52, v246
	s_lshl_b64 s[8:9], s[48:49], 2
	v_and_b32_e32 v7, 31, v52
	v_ashrrev_i32_e32 v6, 6, v52
	s_add_u32 s8, s6, s8
	v_or_b32_e32 v2, s3, v7
	s_addc_u32 s9, s7, s9
	v_lshl_add_u32 v180, v6, 5, v2
	v_mov_b64_e32 v[2:3], s[6:7]
	s_movk_i32 s3, 0x300
	global_load_dword v8, v247, s[8:9] offset:4
	v_mad_i64_i32 v[2:3], s[8:9], v180, s3, v[2:3]
	s_lshl_b32 s8, s37, 7
	s_ashr_i32 s9, s8, 31
	v_lshl_add_u64 v[2:3], v[2:3], 0, s[8:9]
	v_and_b32_e32 v178, 32, v52
	v_lshl_add_u64 v[2:3], v[2:3], 0, v[178:179]
	s_mov_b64 s[8:9], 0x33370100
	s_mov_b32 s3, 0x33370000
	v_lshl_add_u64 v[4:5], v[2:3], 0, s[8:9]
	v_add_co_u32_e32 v2, vcc, s3, v2
	s_mul_i32 s3, s2, 0x82
	s_nop 0
	v_addc_co_u32_e32 v3, vcc, 0, v3, vcc
	global_load_dwordx4 v[138:141], v[2:3], off offset:256
	global_load_dwordx4 v[142:145], v[4:5], off offset:16
	global_load_dwordx4 v[134:137], v[4:5], off offset:80
	global_load_dwordx4 v[130:133], v[4:5], off offset:64
	s_mul_i32 s8, s2, 0x30c000
	s_movk_i32 s2, 0xc00
	s_mul_hi_i32 s9, s3, 0x6000
	v_mul_lo_u32 v50, v6, s2
	s_add_u32 s20, s6, s8
	v_and_b32_e32 v3, 63, v52
	v_bfe_u32 v198, v52, 5, 1
	s_addc_u32 s21, s7, s9
	v_lshlrev_b32_e32 v4, 4, v7
	v_ashrrev_i32_e32 v51, 31, v50
	v_lshl_or_b32 v199, v198, 11, v4
	v_lshl_add_u64 v[4:5], s[20:21], 0, v[50:51]
	v_lshlrev_b32_e32 v178, 4, v3
	v_readfirstlane_b32 s60, v50
	v_lshl_add_u64 v[18:19], v[4:5], 0, v[178:179]
	s_mov_b64 s[20:21], 0x35800100
	s_add_i32 s60, s60, 0
	v_lshl_add_u64 v[4:5], v[18:19], 0, s[20:21]
	s_mov_b32 s2, m0
	s_mov_b32 m0, s60
	s_nop 0
	global_load_lds_dwordx4 v[4:5], off
	s_mov_b32 m0, s2
	s_mov_b64 s[20:21], 0x35800500
	v_lshl_add_u64 v[4:5], v[18:19], 0, s[20:21]
	s_add_i32 s2, s60, 0x400
	s_mov_b32 s3, m0
	s_mov_b32 m0, s2
	s_nop 0
	global_load_lds_dwordx4 v[4:5], off
	s_mov_b32 m0, s3
	s_mov_b64 s[20:21], 0x35800900
	v_lshl_add_u64 v[4:5], v[18:19], 0, s[20:21]
	s_add_i32 s2, s60, 0x800
	s_mov_b32 s3, m0
	s_mov_b32 m0, s2
	s_nop 0
	global_load_lds_dwordx4 v[4:5], off
	s_mov_b32 m0, s3
	s_waitcnt vmcnt(0)
	s_waitcnt lgkmcnt(0)
	s_barrier
; #define LAS __attribute__((address_space(3)))
; #define WAITV(n) asm volatile("s_waitcnt vmcnt(%0)" ::"n"(n) : "memory")
; #define SBAR() do { asm volatile("s_waitcnt lgkmcnt(0)" ::: "memory"); __builtin_amdgcn_s_barrier(); asm volatile("" ::: "memory"); } while (0)
; DEV float ex2(float x) { return __builtin_amdgcn_exp2f(x); }
; #define MFMA8(a, b, c) __builtin_amdgcn_mfma_scale_f32_32x32x64_f8f6f4((a), (b), (c), 0, 0, 0, 0x7f7f7f7f, 0, 0x7c7c7c7c)
; #define MLA_ISSUE(t_, st_) do { const unsigned char* s_ = imgs + (size_t)(t_) * MLA_IMG + wid * (STG / 8) + lane * 16; const unsigned d_ = ldsw + (unsigned)((st_) * STG); \
;     _Pragma("unroll") for (int i_ = 0; i_ < STG / 8192; ++i_) glds16a(s_ + i_ * 1024, d_ + i_ * 1024); } while (0)
; template <int VAR> DEV void mla_unit(const Params& p, int layer, int b, int hd, int tokbase, int t0, int t1, LAS char* lds, SideJob& sj) {
;     ...
;     f32x16 cini, sA0, sA1, sB0, sB1, o0, o1, lacc;
; #pragma unroll
;     for (int i = 0; i < 16; ++i) { cini[i] = cinit; o0[i] = 0.f; o1[i] = 0.f; lacc[i] = 0.f; }
;     const unsigned koffl = (unsigned)(2 * h * 1024 + r * 16);
;     const unsigned voffl = (unsigned)MLA_VOFF + (unsigned)(2 * h * 1024 + r * 16);
;     const int ns = t1 - t0;
;     MLA_ISSUE(t0, 0);
;     WAITV(0); SBAR();
;     if (ns > 1) MLA_ISSUE(t0 + 1, 1);
;     { LAS char* kp = lds + koffl;
;       sA0 = MFMA8(mla_kf8(kp, 0, 0), qf[0], cini); sA1 = MFMA8(mla_kf8(kp, 1, 0), qf[0], cini);
;       sA0 = MFMA8(mla_kf8(kp, 0, 1), qf[1], sA0); sA1 = MFMA8(mla_kf8(kp, 1, 1), qf[1], sA1);
; #pragma unroll
;       for (int i = 0; i < 16; ++i) { sA0[i] = ex2(sA0[i]); sA1[i] = ex2(sA1[i]); } }
;     int slot = 0;
;     v8i pw = {0, 0, 0, 0, 0, 0, 0, 0};
	s_mov_b64 s[20:21], 0x35806100
	v_lshl_add_u64 v[20:21], v[18:19], 0, s[20:21]
	s_add_i32 s2, s60, 0x6000
	s_mov_b32 s3, m0
	s_mov_b32 m0, s2
	s_nop 0
	global_load_lds_dwordx4 v[20:21], off
	s_mov_b32 m0, s3
	s_mov_b64 s[20:21], 0x35806500
	v_lshl_add_u64 v[20:21], v[18:19], 0, s[20:21]
	s_add_i32 s2, s60, 0x6400
	s_mov_b32 s3, m0
	s_mov_b32 m0, s2
	s_nop 0
	global_load_lds_dwordx4 v[20:21], off
	s_mov_b32 m0, s3
	s_mov_b64 s[20:21], 0x35806900
	v_lshl_add_u64 v[18:19], v[18:19], 0, s[20:21]
	s_add_i32 s2, s60, 0x6800
	s_mov_b32 s3, m0
	s_mov_b32 m0, s2
	s_nop 0
	global_load_lds_dwordx4 v[18:19], off
	s_mov_b32 m0, s3
	v_add_u32_e32 v200, 0, v199
	ds_read_b128 v[18:21], v200
	ds_read_b128 v[22:25], v200 offset:1024
	s_waitcnt vmcnt(3)
	v_ashrrev_i32_e32 v191, 4, v52
	s_movk_i32 s2, 0x104
	v_ashrrev_i32_e32 v195, 3, v52
	v_ashrrev_i32_e32 v181, 31, v180
	s_mov_b32 s62, 0
	v_mov_b32_e32 v193, v179
	v_mov_b32_e32 v146, 0
	v_mov_b32_e32 v147, 0
	v_mov_b32_e32 v148, 0
	v_mov_b32_e32 v149, 0
	v_mov_b32_e32 v150, 0
	v_mov_b32_e32 v151, 0
	v_mov_b32_e32 v152, 0
	v_mov_b32_e32 v153, 0
	s_mov_b32 s61, 0
	v_sub_f32_e32 v2, 0x41700000, v8
	v_mov_b32_e32 v3, v2
	v_mov_b32_e32 v4, v2
	v_mov_b32_e32 v5, v2
	v_mov_b32_e32 v6, v2
	v_mov_b32_e32 v7, v2
	v_mov_b32_e32 v8, v2
	v_mov_b32_e32 v9, v2
	v_mov_b32_e32 v10, v2
	v_mov_b32_e32 v11, v2
	v_mov_b32_e32 v12, v2
	v_mov_b32_e32 v13, v2
	v_mov_b32_e32 v14, v2
	v_mov_b32_e32 v15, v2
	v_mov_b32_e32 v16, v2
	v_mov_b32_e32 v17, v2
	s_waitcnt lgkmcnt(0)
	s_nop 0
	v_mfma_scale_f32_32x32x64_f8f6f4 v[18:33], v[18:25], v[138:145], v[2:17], v209, v208 op_sel_hi:[0,0,0]
	ds_read_b128 v[34:37], v200 offset:512
	ds_read_b128 v[38:41], v200 offset:1536
	s_waitcnt lgkmcnt(0)
	v_mfma_scale_f32_32x32x64_f8f6f4 v[34:49], v[34:41], v[138:145], v[2:17], v209, v208 op_sel_hi:[0,0,0]
	ds_read_b128 v[54:57], v200 offset:4096
	ds_read_b128 v[58:61], v200 offset:5120
	s_waitcnt lgkmcnt(0)
	v_mfma_scale_f32_32x32x64_f8f6f4 v[18:33], v[54:61], v[130:137], v[18:33], v209, v208 op_sel_hi:[0,0,0]
	ds_read_b128 v[54:57], v200 offset:4608
	ds_read_b128 v[58:61], v200 offset:5632
	s_waitcnt lgkmcnt(0)
	v_mfma_scale_f32_32x32x64_f8f6f4 v[34:49], v[54:61], v[130:137], v[34:49], v209, v208 op_sel_hi:[0,0,0]
	s_nop 15
	v_exp_f32_e32 v82, v18
	v_lshlrev_b32_e32 v18, 2, v52
	v_and_b32_e32 v190, 60, v18
	v_exp_f32_e32 v83, v19
	v_mul_lo_u32 v18, v191, s2
	s_add_i32 s2, 0, 0x12000
	v_lshlrev_b32_e32 v19, 2, v190
	v_add3_u32 v194, s2, v18, v19
	v_lshlrev_b32_e32 v18, 3, v52
	v_exp_f32_e32 v84, v20
	v_exp_f32_e32 v85, v21
	v_exp_f32_e32 v86, v22
	v_exp_f32_e32 v87, v23
	v_exp_f32_e32 v88, v24
	v_exp_f32_e32 v89, v25
	v_exp_f32_e32 v66, v34
	v_exp_f32_e32 v67, v35
	v_exp_f32_e32 v68, v36
	v_mov_b32_e32 v69, v37
	v_mov_b32_e32 v70, v38
	v_mov_b32_e32 v71, v39
	v_mov_b32_e32 v72, v40
	v_mov_b32_e32 v73, v41
	v_mov_b32_e32 v74, v42
	v_mov_b32_e32 v75, v43
	v_mov_b32_e32 v76, v44
	v_mov_b32_e32 v77, v45
	v_mov_b32_e32 v78, v46
	v_mov_b32_e32 v79, v47
	v_mov_b32_e32 v80, v48
	v_mov_b32_e32 v81, v49
	v_exp_f32_e32 v90, v26
	v_exp_f32_e32 v91, v27
	v_exp_f32_e32 v92, v28
	v_exp_f32_e32 v93, v29
	v_exp_f32_e32 v94, v30
	v_exp_f32_e32 v95, v31
	v_exp_f32_e32 v96, v32
	v_exp_f32_e32 v97, v33
	v_and_b32_e32 v192, 56, v18
	v_or_b32_e32 v18, s8, v178
	v_mov_b32_e32 v19, s9
	v_lshl_add_u64 v[18:19], v[18:19], 0, v[50:51]
	v_lshl_add_u64 v[18:19], s[6:7], 0, v[18:19]
	s_mov_b64 s[8:9], 0x3580c100
	v_mov_b32_e32 v34, 0
	v_cmp_lt_u32_e64 s[40:41], 31, v190
	v_lshl_add_u32 v196, v195, 2, s2
	v_mul_u32_u24_e32 v197, 0x104, v192
	v_lshl_add_u64 v[162:163], v[18:19], 0, s[8:9]
	v_mov_b32_e32 v35, v34
	v_mov_b32_e32 v36, v34
	v_mov_b32_e32 v37, v34
	v_mov_b32_e32 v38, v34
	v_mov_b32_e32 v39, v34
	v_mov_b32_e32 v40, v34
	v_mov_b32_e32 v41, v34
	v_mov_b32_e32 v42, v34
	v_mov_b32_e32 v43, v34
	v_mov_b32_e32 v44, v34
	v_mov_b32_e32 v45, v34
	v_mov_b32_e32 v46, v34
	v_mov_b32_e32 v47, v34
	v_mov_b32_e32 v48, v34
	v_mov_b32_e32 v49, v34
	v_mov_b32_e32 v18, v34
	v_mov_b32_e32 v19, v34
	v_mov_b32_e32 v20, v34
	v_mov_b32_e32 v21, v34
	v_mov_b32_e32 v22, v34
	v_mov_b32_e32 v23, v34
	v_mov_b32_e32 v24, v34
	v_mov_b32_e32 v25, v34
	v_mov_b32_e32 v26, v34
	v_mov_b32_e32 v27, v34
	v_mov_b32_e32 v28, v34
	v_mov_b32_e32 v29, v34
	v_mov_b32_e32 v30, v34
	v_mov_b32_e32 v31, v34
	v_mov_b32_e32 v32, v34
	v_mov_b32_e32 v33, v34
	v_mov_b32_e32 v50, v34
	v_mov_b32_e32 v51, v34
	v_mov_b32_e32 v52, v34
	v_mov_b32_e32 v53, v34
	v_mov_b32_e32 v54, v34
	v_mov_b32_e32 v55, v34
	v_mov_b32_e32 v56, v34
	v_mov_b32_e32 v57, v34
	v_mov_b32_e32 v58, v34
	v_mov_b32_e32 v59, v34
	v_mov_b32_e32 v60, v34
	v_mov_b32_e32 v61, v34
	v_mov_b32_e32 v62, v34
	v_mov_b32_e32 v63, v34
	v_mov_b32_e32 v64, v34
	v_mov_b32_e32 v65, v34
	v_mov_b64_e32 v[210:211], s[76:77]
	v_mov_b64_e32 v[212:213], s[78:79]
	v_mov_b64_e32 v[214:215], s[80:81]
	v_mov_b64_e32 v[216:217], s[82:83]
	s_cmp_ge_u32 s60, 0x3000
	s_cbranch_scc0 .Lmla_prio_skip
	s_setprio 1
.Lmla_prio_skip:
	s_branch .LBB0_813

; #define LAS __attribute__((address_space(3)))
; #define WAITV(n) asm volatile("s_waitcnt vmcnt(%0)" ::"n"(n) : "memory")
; #define SBAR() do { asm volatile("s_waitcnt lgkmcnt(0)" ::: "memory"); __builtin_amdgcn_s_barrier(); asm volatile("" ::: "memory"); } while (0)
; DEV unsigned pk_bf8x4(float a, float b, float c, float d, int old = 0) { int w = __builtin_amdgcn_cvt_pk_bf8_f32(a, b, old, false); w = __builtin_amdgcn_cvt_pk_bf8_f32(c, d, w, true); return (unsigned)w; }
; #define MLA_ISSUE(t_, st_) do { const unsigned char* s_ = imgs + (size_t)(t_) * MLA_IMG + wid * (STG / 8) + lane * 16; const unsigned d_ = ldsw + (unsigned)((st_) * STG); \
;     _Pragma("unroll") for (int i_ = 0; i_ < STG / 8192; ++i_) glds16a(s_ + i_ * 1024, d_ + i_ * 1024); } while (0)
; template <int VAR> DEV void mla_unit(const Params& p, int layer, int b, int hd, int tokbase, int t0, int t1, LAS char* lds, SideJob& sj) {
;     ...
;     for (int s = 0; s < ns; ++s) {
;         sj_tick(p, layer, sj, lds, tid);
;         { LAS char* base = lds + slot * STG; mla_step<VAR>(sB0, sB1, sA0, sA1, o0, o1, lacc, qf, cini, base + MLA_KSUB + koffl, base + voffl, pw); }
;         if (s + 1 < ns) {
;             const int nslot = (slot == 2) ? 0 : slot + 1;
;             WAITV(0); SBAR();
;             if (s + 2 < ns) MLA_ISSUE(t0 + s + 2, (nslot == 2) ? 0 : nslot + 1);
;             { LAS char* nb = lds + nslot * STG; LAS char* ob = lds + slot * STG; mla_step<VAR>(sA0, sA1, sB0, sB1, o0, o1, lacc, qf, cini, nb + koffl, ob + MLA_VSUB + voffl, pw); }
;             slot = nslot;
;         }
;     }
;     {
; #pragma unroll
;       for (int w = 0; w < 8; ++w) { const int e = 4 * w; pw[w] = (int)((e < 16) ? pk_bf8x4(sB0[e], sB0[e + 1], sB0[e + 2], sB0[e + 3]) : pk_bf8x4(sB1[e - 16], sB1[e - 15], sB1[e - 14], sB1[e - 13])); }
.LBB0_835:
	s_setprio 0
	v_exp_f32_e32 v69, v69
	v_exp_f32_e32 v70, v70
	v_exp_f32_e32 v71, v71
	v_exp_f32_e32 v72, v72
	v_exp_f32_e32 v73, v73
	v_exp_f32_e32 v74, v74
	v_exp_f32_e32 v75, v75
	v_exp_f32_e32 v76, v76
	v_exp_f32_e32 v77, v77
	v_exp_f32_e32 v78, v78
	v_exp_f32_e32 v79, v79
	v_exp_f32_e32 v80, v80
	v_exp_f32_e32 v81, v81
	s_add_i32 s2, s29, s61
	s_and_b32 s66, s2, 3
	s_cmp_gt_i32 s33, 63
	s_cselect_b64 s[20:21], -1, 0
	s_cmp_eq_u32 s66, 3
	s_cselect_b64 s[50:51], -1, 0
	s_or_b64 s[20:21], s[20:21], s[50:51]
	s_and_b64 vcc, exec, s[20:21]
	s_cbranch_vccnz .LBB0_858
	s_add_i32 s50, s33, s12
	s_cmpk_lt_i32 s36, 0x100
	s_cselect_b64 s[52:53], -1, 0
	s_lshl_b32 s60, s36, 6
	s_cmpk_gt_i32 s36, 0xff
	s_mov_b64 s[58:59], -1
	s_cbranch_scc1 .LBB0_838
	s_ashr_i32 s51, s50, 31
	s_lshl_b64 s[54:55], s[50:51], 21
	s_add_u32 s20, s44, s54
	s_addc_u32 s21, s45, s55
	s_add_u32 s54, s46, s54
	s_addc_u32 s55, s47, s55
	s_lshl_b64 s[56:57], s[50:51], 20
	s_add_u32 s56, s13, s56
	s_addc_u32 s57, s16, s57
	s_and_b32 s30, s60, 0x3c0
	s_ashr_i32 s65, s36, 4
	s_mov_b64 s[58:59], 0
